# P7 merged-output stores nt
# baseline (speedup 1.0000x reference)
.LBB0_1047:
	s_lshl_b32 s4, s64, 8
	v_mov_b32_e32 v148, v0
	s_add_i32 s4, s4, s58
	s_mov_b32 s12, 0x20000
	v_and_or_b32 v212, v148, 15, s4
	s_lshl_b32 s4, s63, 6
	s_or_b32 s4, s4, s61
	v_lshrrev_b32_e32 v2, 2, v148
	v_and_or_b32 v214, v2, 12, s4
	v_ashrrev_i32_e32 v213, 31, v212
	v_lshl_add_u64 v[246:247], v[212:213], 2, s[20:21]
	global_load_dword v232, v[246:247], off
	global_load_dword v231, v[246:247], off offset:64
	global_load_dword v230, v[246:247], off offset:128
	global_load_dword v229, v[246:247], off offset:192
	global_load_dword v228, v[246:247], off offset:512
	global_load_dword v227, v[246:247], off offset:576
	global_load_dword v226, v[246:247], off offset:640
	global_load_dword v225, v[246:247], off offset:704
	v_ashrrev_i32_e32 v140, 3, v214
	v_lshlrev_b64 v[144:145], 3, v[212:213]
	v_ashrrev_i32_e32 v141, 31, v140
	v_and_b32_e32 v147, 0x3fffff, v145
	v_and_b32_e32 v146, 0xfffffe00, v144
	v_lshl_add_u64 v[146:147], v[146:147], 0, v[140:141]
	v_lshlrev_b64 v[146:147], 10, v[146:147]
	v_lshlrev_b32_e32 v2, 1, v144
	v_lshl_add_u64 v[146:147], s[18:19], 0, v[146:147]
	v_and_b32_e32 v2, 0xf0, v2
	v_lshl_add_u64 v[144:145], v[146:147], 0, v[2:3]
	v_lshrrev_b32_e32 v2, 1, v148
	v_or_b32_e32 v194, 16, v212
	v_and_b32_e32 v2, 8, v2
	v_ashrrev_i32_e32 v195, 31, v194
	v_lshl_add_u64 v[144:145], v[144:145], 0, v[2:3]
	v_lshlrev_b64 v[154:155], 3, v[194:195]
	v_add_co_u32_e32 v146, vcc, s12, v144
	v_and_b32_e32 v157, 0x3fffff, v155
	v_and_b32_e32 v156, 0xfffffe00, v154
	v_addc_co_u32_e32 v147, vcc, 0, v145, vcc
	s_mov_b32 s5, 0x40000
	v_lshl_add_u64 v[156:157], v[156:157], 0, v[140:141]
	v_add_co_u32_e32 v148, vcc, s5, v144
	v_lshlrev_b64 v[156:157], 10, v[156:157]
	v_lshlrev_b32_e32 v154, 1, v154
	v_addc_co_u32_e32 v149, vcc, 0, v145, vcc
	s_mov_b32 s4, 0x60000
	v_lshl_add_u64 v[156:157], s[18:19], 0, v[156:157]
	v_and_b32_e32 v154, 0x3f0, v154
	v_mov_b32_e32 v155, v3
	v_add_co_u32_e32 v150, vcc, s4, v144
	v_lshl_add_u64 v[154:155], v[156:157], 0, v[154:155]
	s_nop 0
	v_addc_co_u32_e32 v151, vcc, 0, v145, vcc
	v_lshl_add_u64 v[154:155], v[154:155], 0, v[2:3]
	v_lshl_add_u64 v[152:153], v[194:195], 2, s[20:21]
	global_load_dwordx2 v[218:219], v[148:149], off nt
	global_load_dwordx2 v[216:217], v[150:151], off nt
	global_load_dwordx2 v[204:205], v[154:155], off nt
	v_add_co_u32_e32 v148, vcc, s12, v154
	v_or_b32_e32 v184, 32, v212
	s_nop 0
	v_addc_co_u32_e32 v149, vcc, 0, v155, vcc
	v_add_co_u32_e32 v150, vcc, s5, v154
	v_ashrrev_i32_e32 v185, 31, v184
	s_nop 0
	v_addc_co_u32_e32 v151, vcc, 0, v155, vcc
	v_add_co_u32_e32 v152, vcc, s4, v154
	v_or_b32_e32 v174, 48, v212
	s_nop 0
	v_addc_co_u32_e32 v153, vcc, 0, v155, vcc
	v_lshl_add_u64 v[154:155], v[184:185], 2, s[20:21]
	global_load_dwordx2 v[210:211], v[148:149], off nt
	global_load_dwordx2 v[208:209], v[150:151], off nt
	global_load_dwordx2 v[206:207], v[152:153], off nt
	v_lshlrev_b64 v[148:149], 3, v[184:185]
	v_and_b32_e32 v151, 0x3fffff, v149
	v_and_b32_e32 v150, 0xfffffe00, v148
	v_lshl_add_u64 v[150:151], v[150:151], 0, v[140:141]
	v_lshlrev_b64 v[150:151], 10, v[150:151]
	v_lshlrev_b32_e32 v148, 1, v148
	v_lshl_add_u64 v[150:151], s[18:19], 0, v[150:151]
	v_and_b32_e32 v148, 0x3f0, v148
	v_mov_b32_e32 v149, v3
	v_lshl_add_u64 v[148:149], v[150:151], 0, v[148:149]
	v_lshl_add_u64 v[148:149], v[148:149], 0, v[2:3]
	v_add_co_u32_e32 v150, vcc, s12, v148
	v_ashrrev_i32_e32 v175, 31, v174
	s_nop 0
	v_addc_co_u32_e32 v151, vcc, 0, v149, vcc
	v_add_co_u32_e32 v152, vcc, s5, v148
	v_lshl_add_u64 v[142:143], v[212:213], 2, s[20:21]
	s_nop 0
	v_addc_co_u32_e32 v153, vcc, 0, v149, vcc
	v_add_co_u32_e32 v154, vcc, s4, v148
	v_add_u32_e32 v164, 0x80, v212
	s_nop 0
	v_addc_co_u32_e32 v155, vcc, 0, v149, vcc
	global_load_dwordx2 v[192:193], v[148:149], off nt
	global_load_dwordx2 v[190:191], v[150:151], off nt
	global_load_dwordx2 v[188:189], v[152:153], off nt
	global_load_dwordx2 v[186:187], v[154:155], off nt
	v_lshlrev_b64 v[150:151], 3, v[174:175]
	v_and_b32_e32 v153, 0x3fffff, v151
	v_and_b32_e32 v152, 0xfffffe00, v150
	v_lshl_add_u64 v[152:153], v[152:153], 0, v[140:141]
	v_lshlrev_b64 v[152:153], 10, v[152:153]
	v_lshlrev_b32_e32 v150, 1, v150
	v_lshl_add_u64 v[152:153], s[18:19], 0, v[152:153]
	v_and_b32_e32 v150, 0x3f0, v150
	v_mov_b32_e32 v151, v3
	v_lshl_add_u64 v[150:151], v[152:153], 0, v[150:151]
	v_lshl_add_u64 v[150:151], v[150:151], 0, v[2:3]
	v_add_co_u32_e32 v152, vcc, s12, v150
	v_lshl_add_u64 v[148:149], v[174:175], 2, s[20:21]
	s_nop 0
	v_addc_co_u32_e32 v153, vcc, 0, v151, vcc
	v_add_co_u32_e32 v154, vcc, s5, v150
	v_ashrrev_i32_e32 v165, 31, v164
	s_nop 0
	v_addc_co_u32_e32 v155, vcc, 0, v151, vcc
	global_load_dwordx2 v[180:181], v[150:151], off nt
	global_load_dwordx2 v[178:179], v[152:153], off nt
	global_load_dwordx2 v[176:177], v[154:155], off nt
	global_load_dwordx2 v[222:223], v[144:145], off nt
	global_load_dwordx2 v[220:221], v[146:147], off nt
	v_lshlrev_b64 v[142:143], 3, v[164:165]
	v_and_b32_e32 v145, 0x3fffff, v143
	v_and_b32_e32 v144, 0xfffffe00, v142
	v_lshl_add_u64 v[144:145], v[144:145], 0, v[140:141]
	v_lshlrev_b64 v[144:145], 10, v[144:145]
	v_lshlrev_b32_e32 v142, 1, v142
	v_lshl_add_u64 v[144:145], s[18:19], 0, v[144:145]
	v_and_b32_e32 v142, 0x3f0, v142
	v_mov_b32_e32 v143, v3
	v_add_co_u32_e32 v148, vcc, s4, v150
	v_lshl_add_u64 v[142:143], v[144:145], 0, v[142:143]
	s_nop 0
	v_addc_co_u32_e32 v149, vcc, 0, v151, vcc
	v_lshl_add_u64 v[142:143], v[142:143], 0, v[2:3]
	v_add_co_u32_e32 v144, vcc, s12, v142
	v_add_u32_e32 v196, 0xb0, v212
	s_nop 0
	v_addc_co_u32_e32 v145, vcc, 0, v143, vcc
	v_add_co_u32_e32 v146, vcc, s5, v142
	v_ashrrev_i32_e32 v197, 31, v196
	s_nop 0
	v_addc_co_u32_e32 v147, vcc, 0, v143, vcc
	global_load_dwordx2 v[182:183], v[148:149], off nt
	global_load_dwordx2 v[170:171], v[142:143], off nt
	global_load_dwordx2 v[168:169], v[144:145], off nt
	global_load_dwordx2 v[166:167], v[146:147], off nt
	v_add_u32_e32 v144, 0x90, v212
	v_ashrrev_i32_e32 v145, 31, v144
	v_lshl_add_u64 v[146:147], v[144:145], 2, s[20:21]
	v_lshlrev_b64 v[144:145], 3, v[144:145]
	v_and_b32_e32 v149, 0x3fffff, v145
	v_and_b32_e32 v148, 0xfffffe00, v144
	v_lshl_add_u64 v[148:149], v[148:149], 0, v[140:141]
	v_lshlrev_b64 v[148:149], 10, v[148:149]
	v_lshlrev_b32_e32 v144, 1, v144
	v_lshl_add_u64 v[148:149], s[18:19], 0, v[148:149]
	v_and_b32_e32 v144, 0x3f0, v144
	v_mov_b32_e32 v145, v3
	v_add_co_u32_e32 v142, vcc, s4, v142
	v_lshl_add_u64 v[144:145], v[148:149], 0, v[144:145]
	s_nop 0
	v_addc_co_u32_e32 v143, vcc, 0, v143, vcc
	v_lshl_add_u64 v[144:145], v[144:145], 0, v[2:3]
	v_add_co_u32_e32 v148, vcc, s12, v144
	v_lshl_add_u64 v[198:199], v[196:197], 2, s[20:21]
	s_nop 0
	v_addc_co_u32_e32 v149, vcc, 0, v145, vcc
	global_load_dwordx2 v[172:173], v[142:143], off nt
	global_load_dwordx2 v[158:159], v[144:145], off nt
	global_load_dwordx2 v[156:157], v[148:149], off nt
	v_add_u32_e32 v146, 0xa0, v212
	v_ashrrev_i32_e32 v147, 31, v146
	v_lshl_add_u64 v[148:149], v[146:147], 2, s[20:21]
	v_lshlrev_b64 v[146:147], 3, v[146:147]
	v_and_b32_e32 v151, 0x3fffff, v147
	v_and_b32_e32 v150, 0xfffffe00, v146
	v_lshl_add_u64 v[150:151], v[150:151], 0, v[140:141]
	v_add_co_u32_e32 v142, vcc, s5, v144
	v_lshlrev_b64 v[150:151], 10, v[150:151]
	v_lshlrev_b32_e32 v146, 1, v146
	v_addc_co_u32_e32 v143, vcc, 0, v145, vcc
	v_lshl_add_u64 v[150:151], s[18:19], 0, v[150:151]
	v_and_b32_e32 v146, 0x3f0, v146
	v_mov_b32_e32 v147, v3
	v_add_co_u32_e32 v144, vcc, s4, v144
	v_lshl_add_u64 v[146:147], v[150:151], 0, v[146:147]
	s_nop 0
	v_addc_co_u32_e32 v145, vcc, 0, v145, vcc
	v_lshl_add_u64 v[146:147], v[146:147], 0, v[2:3]
	global_load_dwordx2 v[162:163], v[142:143], off nt
	global_load_dwordx2 v[160:161], v[144:145], off nt
	s_nop 0
	global_load_dwordx2 v[148:149], v[146:147], off nt
	v_add_co_u32_e32 v142, vcc, s12, v146
	s_waitcnt vmcnt(25)
	v_mul_f32_e32 v225, 0xbfb8aa3b, v225
	v_mul_f32_e32 v226, 0xbfb8aa3b, v226
	v_mul_f32_e32 v227, 0xbfb8aa3b, v227
	v_mul_f32_e32 v228, 0xbfb8aa3b, v228
	v_mul_f32_e32 v229, 0xbfb8aa3b, v229
	v_mul_f32_e32 v230, 0xbfb8aa3b, v230
	v_mul_f32_e32 v231, 0xbfb8aa3b, v231
	v_mul_f32_e32 v232, 0xbfb8aa3b, v232
	v_mul_f32_e32 v108, v231, v108
	v_addc_co_u32_e32 v143, vcc, 0, v147, vcc
	v_add_co_u32_e32 v144, vcc, s5, v146
	v_mul_f32_e32 v124, v232, v124
	s_nop 0
	v_addc_co_u32_e32 v145, vcc, 0, v147, vcc
	v_add_co_u32_e32 v146, vcc, s4, v146
	s_nop 0
	v_addc_co_u32_e32 v147, vcc, 0, v147, vcc
	global_load_dwordx2 v[154:155], v[142:143], off nt
	global_load_dwordx2 v[152:153], v[144:145], off nt
	global_load_dwordx2 v[150:151], v[146:147], off nt
	v_lshlrev_b64 v[142:143], 3, v[196:197]
	v_and_b32_e32 v145, 0x3fffff, v143
	v_and_b32_e32 v144, 0xfffffe00, v142
	v_lshl_add_u64 v[140:141], v[144:145], 0, v[140:141]
	v_lshlrev_b64 v[140:141], 10, v[140:141]
	v_lshlrev_b32_e32 v142, 1, v142
	v_lshl_add_u64 v[140:141], s[18:19], 0, v[140:141]
	v_and_b32_e32 v142, 0x3f0, v142
	v_mov_b32_e32 v143, v3
	v_lshl_add_u64 v[140:141], v[140:141], 0, v[142:143]
	v_lshl_add_u64 v[140:141], v[140:141], 0, v[2:3]
	v_mul_f32_e32 v2, v232, v128
	v_mul_f32_e32 v128, v232, v129
	v_exp_f32_e32 v2, v2
	v_exp_f32_e32 v129, v128
	v_mul_f32_e32 v125, v232, v125
	v_add_f32_e32 v2, 1.0, v2
	v_rcp_f32_e32 v128, v2
	v_add_f32_e32 v2, 1.0, v129
	v_mul_f32_e32 v129, v232, v130
	v_exp_f32_e32 v130, v129
	v_mul_f32_e32 v129, v232, v131
	v_exp_f32_e32 v131, v129
	v_exp_f32_e32 v124, v124
	v_exp_f32_e32 v125, v125
	v_rcp_f32_e32 v129, v2
	v_add_f32_e32 v2, 1.0, v130
	v_rcp_f32_e32 v130, v2
	v_add_f32_e32 v2, 1.0, v131
	v_rcp_f32_e32 v131, v2
	v_add_f32_e32 v2, 1.0, v124
	v_rcp_f32_e32 v124, v2
	v_add_f32_e32 v2, 1.0, v125
	v_mul_f32_e32 v125, v232, v126
	v_exp_f32_e32 v126, v125
	v_mul_f32_e32 v125, v232, v127
	v_mul_f32_e32 v120, v232, v120
	v_exp_f32_e32 v127, v125
	v_mul_f32_e32 v121, v232, v121
	v_exp_f32_e32 v120, v120
	v_exp_f32_e32 v121, v121
	v_rcp_f32_e32 v125, v2
	v_add_f32_e32 v2, 1.0, v126
	v_rcp_f32_e32 v126, v2
	v_add_f32_e32 v2, 1.0, v127
	v_rcp_f32_e32 v127, v2
	v_add_f32_e32 v2, 1.0, v120
	v_rcp_f32_e32 v120, v2
	v_add_f32_e32 v2, 1.0, v121
	v_mul_f32_e32 v121, v232, v122
	v_exp_f32_e32 v122, v121
	v_mul_f32_e32 v121, v232, v123
	v_mul_f32_e32 v116, v232, v116
	v_exp_f32_e32 v123, v121
	v_mul_f32_e32 v117, v232, v117
	v_exp_f32_e32 v116, v116
	v_exp_f32_e32 v117, v117
	v_rcp_f32_e32 v121, v2
	v_add_f32_e32 v2, 1.0, v122
	v_rcp_f32_e32 v122, v2
	v_add_f32_e32 v2, 1.0, v123
	v_rcp_f32_e32 v123, v2
	v_add_f32_e32 v2, 1.0, v116
	v_rcp_f32_e32 v116, v2
	v_add_f32_e32 v2, 1.0, v117
	v_rcp_f32_e32 v117, v2
	v_mul_f32_e32 v2, v232, v118
	v_mul_f32_e32 v118, v232, v119
	v_exp_f32_e32 v2, v2
	v_exp_f32_e32 v119, v118
	v_add_f32_e32 v2, 1.0, v2
	v_rcp_f32_e32 v118, v2
	v_add_f32_e32 v2, 1.0, v119
	v_rcp_f32_e32 v119, v2
	v_mul_f32_e32 v2, v231, v112
	v_mul_f32_e32 v112, v231, v113
	v_exp_f32_e32 v2, v2
	v_exp_f32_e32 v113, v112
	v_mul_f32_e32 v109, v231, v109
	v_add_f32_e32 v2, 1.0, v2
	v_rcp_f32_e32 v112, v2
	v_add_f32_e32 v2, 1.0, v113
	v_mul_f32_e32 v113, v231, v114
	v_exp_f32_e32 v114, v113
	v_mul_f32_e32 v113, v231, v115
	v_exp_f32_e32 v115, v113
	v_exp_f32_e32 v108, v108
	v_exp_f32_e32 v109, v109
	v_rcp_f32_e32 v113, v2
	v_add_f32_e32 v2, 1.0, v114
	v_rcp_f32_e32 v114, v2
	v_add_f32_e32 v2, 1.0, v115
	v_rcp_f32_e32 v115, v2
	v_add_f32_e32 v2, 1.0, v108
	v_rcp_f32_e32 v108, v2
	v_add_f32_e32 v2, 1.0, v109
	v_mul_f32_e32 v109, v231, v110
	v_exp_f32_e32 v110, v109
	v_mul_f32_e32 v109, v231, v111
	v_mul_f32_e32 v104, v231, v104
	v_exp_f32_e32 v111, v109
	v_mul_f32_e32 v105, v231, v105
	v_exp_f32_e32 v104, v104
	v_exp_f32_e32 v105, v105
	v_rcp_f32_e32 v109, v2
	v_add_f32_e32 v2, 1.0, v110
	v_rcp_f32_e32 v110, v2
	v_add_f32_e32 v2, 1.0, v111
	v_rcp_f32_e32 v111, v2
	v_add_f32_e32 v2, 1.0, v104
	v_rcp_f32_e32 v104, v2
	v_add_f32_e32 v2, 1.0, v105
	v_mul_f32_e32 v105, v231, v106
	v_exp_f32_e32 v106, v105
	v_mul_f32_e32 v105, v231, v107
	v_mul_f32_e32 v100, v231, v100
	v_exp_f32_e32 v107, v105
	v_mul_f32_e32 v101, v231, v101
	v_exp_f32_e32 v100, v100
	v_exp_f32_e32 v101, v101
	v_rcp_f32_e32 v105, v2
	v_add_f32_e32 v2, 1.0, v106
	v_rcp_f32_e32 v106, v2
	v_add_f32_e32 v2, 1.0, v107
	v_rcp_f32_e32 v107, v2
	v_add_f32_e32 v2, 1.0, v100
	v_rcp_f32_e32 v100, v2
	v_add_f32_e32 v2, 1.0, v101
	v_rcp_f32_e32 v101, v2
	v_mul_f32_e32 v2, v231, v102
	v_mul_f32_e32 v102, v231, v103
	v_exp_f32_e32 v2, v2
	v_exp_f32_e32 v103, v102
	v_mul_f32_e32 v92, v230, v92
	v_add_f32_e32 v2, 1.0, v2
	v_rcp_f32_e32 v102, v2
	v_add_f32_e32 v2, 1.0, v103
	v_rcp_f32_e32 v103, v2
	v_mul_f32_e32 v2, v230, v96
	v_mul_f32_e32 v96, v230, v97
	v_exp_f32_e32 v2, v2
	v_exp_f32_e32 v97, v96
	v_add_f32_e32 v2, 1.0, v2
	v_rcp_f32_e32 v96, v2
	v_add_f32_e32 v2, 1.0, v97
	v_mul_f32_e32 v97, v230, v98
	v_exp_f32_e32 v98, v97
	v_mul_f32_e32 v97, v230, v99
	v_exp_f32_e32 v99, v97
	v_mul_f32_e32 v93, v230, v93
	v_exp_f32_e32 v92, v92
	v_exp_f32_e32 v93, v93
	v_rcp_f32_e32 v97, v2
	v_add_f32_e32 v2, 1.0, v98
	v_rcp_f32_e32 v98, v2
	v_add_f32_e32 v2, 1.0, v99
	v_rcp_f32_e32 v99, v2
	v_add_f32_e32 v2, 1.0, v92
	v_rcp_f32_e32 v92, v2
	v_add_f32_e32 v2, 1.0, v93
	v_mul_f32_e32 v93, v230, v94
	v_exp_f32_e32 v94, v93
	v_mul_f32_e32 v93, v230, v95
	v_mul_f32_e32 v88, v230, v88
	v_exp_f32_e32 v95, v93
	v_mul_f32_e32 v89, v230, v89
	v_exp_f32_e32 v88, v88
	v_exp_f32_e32 v89, v89
	v_rcp_f32_e32 v93, v2
	v_add_f32_e32 v2, 1.0, v94
	v_rcp_f32_e32 v94, v2
	v_add_f32_e32 v2, 1.0, v95
	v_rcp_f32_e32 v95, v2
	v_add_f32_e32 v2, 1.0, v88
	v_rcp_f32_e32 v88, v2
	v_add_f32_e32 v2, 1.0, v89
	v_mul_f32_e32 v89, v230, v90
	v_exp_f32_e32 v90, v89
	v_mul_f32_e32 v89, v230, v91
	v_mul_f32_e32 v84, v230, v84
	v_exp_f32_e32 v91, v89
	v_mul_f32_e32 v85, v230, v85
	v_exp_f32_e32 v84, v84
	v_exp_f32_e32 v85, v85
	v_rcp_f32_e32 v89, v2
	v_add_f32_e32 v2, 1.0, v90
	v_rcp_f32_e32 v90, v2
	v_add_f32_e32 v2, 1.0, v91
	v_rcp_f32_e32 v91, v2
	v_add_f32_e32 v2, 1.0, v84
	v_rcp_f32_e32 v84, v2
	v_add_f32_e32 v2, 1.0, v85
	v_rcp_f32_e32 v85, v2
	v_mul_f32_e32 v2, v230, v86
	v_mul_f32_e32 v86, v230, v87
	v_exp_f32_e32 v2, v2
	v_exp_f32_e32 v87, v86
	v_mul_f32_e32 v76, v229, v76
	v_add_f32_e32 v2, 1.0, v2
	v_rcp_f32_e32 v86, v2
	v_add_f32_e32 v2, 1.0, v87
	v_rcp_f32_e32 v87, v2
	v_mul_f32_e32 v2, v229, v80
	v_mul_f32_e32 v80, v229, v81
	v_exp_f32_e32 v2, v2
	v_exp_f32_e32 v81, v80
	v_add_f32_e32 v2, 1.0, v2
	v_rcp_f32_e32 v80, v2
	v_add_f32_e32 v2, 1.0, v81
	v_mul_f32_e32 v81, v229, v82
	v_exp_f32_e32 v82, v81
	v_mul_f32_e32 v81, v229, v83
	v_exp_f32_e32 v83, v81
	v_mul_f32_e32 v77, v229, v77
	v_exp_f32_e32 v76, v76
	v_exp_f32_e32 v77, v77
	v_rcp_f32_e32 v81, v2
	v_add_f32_e32 v2, 1.0, v82
	v_rcp_f32_e32 v82, v2
	v_add_f32_e32 v2, 1.0, v83
	v_rcp_f32_e32 v83, v2
	v_add_f32_e32 v2, 1.0, v76
	v_rcp_f32_e32 v76, v2
	v_add_f32_e32 v2, 1.0, v77
	v_mul_f32_e32 v77, v229, v78
	v_exp_f32_e32 v78, v77
	v_mul_f32_e32 v77, v229, v79
	v_mul_f32_e32 v72, v229, v72
	v_exp_f32_e32 v79, v77
	v_mul_f32_e32 v73, v229, v73
	v_exp_f32_e32 v72, v72
	v_exp_f32_e32 v73, v73
	v_rcp_f32_e32 v77, v2
	v_add_f32_e32 v2, 1.0, v78
	v_rcp_f32_e32 v78, v2
	v_add_f32_e32 v2, 1.0, v79
	v_rcp_f32_e32 v79, v2
	v_add_f32_e32 v2, 1.0, v72
	v_rcp_f32_e32 v72, v2
	v_add_f32_e32 v2, 1.0, v73
	v_mul_f32_e32 v73, v229, v74
	v_exp_f32_e32 v74, v73
	v_mul_f32_e32 v73, v229, v75
	v_mul_f32_e32 v68, v229, v68
	v_exp_f32_e32 v75, v73
	v_mul_f32_e32 v69, v229, v69
	v_exp_f32_e32 v68, v68
	v_exp_f32_e32 v69, v69
	v_rcp_f32_e32 v73, v2
	v_add_f32_e32 v2, 1.0, v74
	v_rcp_f32_e32 v74, v2
	v_add_f32_e32 v2, 1.0, v75
	v_rcp_f32_e32 v75, v2
	v_add_f32_e32 v2, 1.0, v68
	v_rcp_f32_e32 v68, v2
	v_add_f32_e32 v2, 1.0, v69
	v_rcp_f32_e32 v69, v2
	v_mul_f32_e32 v2, v229, v70
	v_mul_f32_e32 v70, v229, v71
	v_exp_f32_e32 v2, v2
	v_exp_f32_e32 v71, v70
	v_mul_f32_e32 v60, v228, v60
	v_add_f32_e32 v2, 1.0, v2
	v_rcp_f32_e32 v70, v2
	v_add_f32_e32 v2, 1.0, v71
	v_rcp_f32_e32 v71, v2
	v_mul_f32_e32 v2, v228, v64
	v_mul_f32_e32 v64, v228, v65
	v_exp_f32_e32 v2, v2
	v_exp_f32_e32 v65, v64
	v_add_f32_e32 v2, 1.0, v2
	v_rcp_f32_e32 v64, v2
	v_add_f32_e32 v2, 1.0, v65
	v_mul_f32_e32 v65, v228, v66
	v_exp_f32_e32 v66, v65
	v_mul_f32_e32 v65, v228, v67
	v_exp_f32_e32 v67, v65
	v_mul_f32_e32 v61, v228, v61
	v_exp_f32_e32 v60, v60
	v_exp_f32_e32 v61, v61
	v_rcp_f32_e32 v65, v2
	v_add_f32_e32 v2, 1.0, v66
	v_rcp_f32_e32 v66, v2
	v_add_f32_e32 v2, 1.0, v67
	v_rcp_f32_e32 v67, v2
	v_add_f32_e32 v2, 1.0, v60
	v_rcp_f32_e32 v60, v2
	v_add_f32_e32 v2, 1.0, v61
	v_mul_f32_e32 v61, v228, v62
	v_exp_f32_e32 v62, v61
	v_mul_f32_e32 v61, v228, v63
	v_mul_f32_e32 v56, v228, v56
	v_exp_f32_e32 v63, v61
	v_mul_f32_e32 v57, v228, v57
	v_exp_f32_e32 v56, v56
	v_exp_f32_e32 v57, v57
	v_rcp_f32_e32 v61, v2
	v_add_f32_e32 v2, 1.0, v62
	v_rcp_f32_e32 v62, v2
	v_add_f32_e32 v2, 1.0, v63
	v_rcp_f32_e32 v63, v2
	v_add_f32_e32 v2, 1.0, v56
	v_rcp_f32_e32 v56, v2
	v_add_f32_e32 v2, 1.0, v57
	v_mul_f32_e32 v57, v228, v58
	v_exp_f32_e32 v58, v57
	v_mul_f32_e32 v57, v228, v59
	v_mul_f32_e32 v52, v228, v52
	v_exp_f32_e32 v59, v57
	v_mul_f32_e32 v53, v228, v53
	v_exp_f32_e32 v52, v52
	v_exp_f32_e32 v53, v53
	v_rcp_f32_e32 v57, v2
	v_add_f32_e32 v2, 1.0, v58
	v_rcp_f32_e32 v58, v2
	v_add_f32_e32 v2, 1.0, v59
	v_rcp_f32_e32 v59, v2
	v_add_f32_e32 v2, 1.0, v52
	v_rcp_f32_e32 v52, v2
	v_add_f32_e32 v2, 1.0, v53
	v_rcp_f32_e32 v53, v2
	v_mul_f32_e32 v2, v228, v54
	v_mul_f32_e32 v54, v228, v55
	v_exp_f32_e32 v2, v2
	v_exp_f32_e32 v55, v54
	v_mul_f32_e32 v44, v227, v44
	v_add_f32_e32 v2, 1.0, v2
	v_rcp_f32_e32 v54, v2
	v_add_f32_e32 v2, 1.0, v55
	v_rcp_f32_e32 v55, v2
	v_mul_f32_e32 v2, v227, v48
	v_mul_f32_e32 v48, v227, v49
	v_exp_f32_e32 v2, v2
	v_exp_f32_e32 v49, v48
	v_add_f32_e32 v2, 1.0, v2
	v_rcp_f32_e32 v48, v2
	v_add_f32_e32 v2, 1.0, v49
	v_mul_f32_e32 v49, v227, v50
	v_exp_f32_e32 v50, v49
	v_mul_f32_e32 v49, v227, v51
	v_exp_f32_e32 v51, v49
	v_mul_f32_e32 v45, v227, v45
	v_exp_f32_e32 v44, v44
	v_exp_f32_e32 v45, v45
	v_rcp_f32_e32 v49, v2
	v_add_f32_e32 v2, 1.0, v50
	v_rcp_f32_e32 v50, v2
	v_add_f32_e32 v2, 1.0, v51
	v_rcp_f32_e32 v51, v2
	v_add_f32_e32 v2, 1.0, v44
	v_rcp_f32_e32 v44, v2
	v_add_f32_e32 v2, 1.0, v45
	v_mul_f32_e32 v45, v227, v46
	v_exp_f32_e32 v46, v45
	v_mul_f32_e32 v45, v227, v47
	v_mul_f32_e32 v40, v227, v40
	v_exp_f32_e32 v47, v45
	v_mul_f32_e32 v41, v227, v41
	v_exp_f32_e32 v40, v40
	v_exp_f32_e32 v41, v41
	v_rcp_f32_e32 v45, v2
	v_add_f32_e32 v2, 1.0, v46
	v_rcp_f32_e32 v46, v2
	v_add_f32_e32 v2, 1.0, v47
	v_rcp_f32_e32 v47, v2
	v_add_f32_e32 v2, 1.0, v40
	v_rcp_f32_e32 v40, v2
	v_add_f32_e32 v2, 1.0, v41
	v_mul_f32_e32 v41, v227, v42
	v_exp_f32_e32 v42, v41
	v_mul_f32_e32 v41, v227, v43
	v_mul_f32_e32 v36, v227, v36
	v_exp_f32_e32 v43, v41
	v_mul_f32_e32 v37, v227, v37
	v_exp_f32_e32 v36, v36
	v_exp_f32_e32 v37, v37
	v_rcp_f32_e32 v41, v2
	v_add_f32_e32 v2, 1.0, v42
	v_rcp_f32_e32 v42, v2
	v_add_f32_e32 v2, 1.0, v43
	v_rcp_f32_e32 v43, v2
	v_add_f32_e32 v2, 1.0, v36
	v_rcp_f32_e32 v36, v2
	v_add_f32_e32 v2, 1.0, v37
	v_rcp_f32_e32 v37, v2
	v_mul_f32_e32 v2, v227, v38
	v_mul_f32_e32 v38, v227, v39
	v_exp_f32_e32 v2, v2
	v_exp_f32_e32 v39, v38
	s_waitcnt vmcnt(0)
	v_add_co_u32_e32 v142, vcc, s12, v140
	v_add_f32_e32 v2, 1.0, v2
	v_rcp_f32_e32 v38, v2
	v_add_f32_e32 v2, 1.0, v39
	v_rcp_f32_e32 v39, v2
	v_mul_f32_e32 v2, v226, v32
	v_mul_f32_e32 v32, v226, v33
	v_exp_f32_e32 v2, v2
	v_addc_co_u32_e32 v143, vcc, 0, v141, vcc
	v_exp_f32_e32 v33, v32
	v_add_co_u32_e32 v196, vcc, s5, v140
	v_add_f32_e32 v2, 1.0, v2
	s_nop 0
	v_addc_co_u32_e32 v197, vcc, 0, v141, vcc
	v_add_co_u32_e32 v198, vcc, s4, v140
	v_rcp_f32_e32 v32, v2
	s_nop 0
	v_addc_co_u32_e32 v199, vcc, 0, v141, vcc
	global_load_dwordx2 v[146:147], v[140:141], off nt
	global_load_dwordx2 v[144:145], v[142:143], off nt
	s_nop 0
	global_load_dwordx2 v[142:143], v[196:197], off nt
	global_load_dwordx2 v[140:141], v[198:199], off nt
	v_lshlrev_b32_e32 v196, 16, v222
	v_and_b32_e32 v197, 0xffff0000, v222
	v_add_f32_e32 v2, 1.0, v33
	v_mul_f32_e32 v33, v226, v34
	v_pk_fma_f32 v[128:129], v[128:129], v[196:197], 0 op_sel_hi:[1,1,0]
	v_lshlrev_b32_e32 v196, 16, v220
	v_and_b32_e32 v197, 0xffff0000, v220
	v_pk_fma_f32 v[124:125], v[124:125], v[196:197], v[128:129]
	v_lshlrev_b32_e32 v128, 16, v218
	v_and_b32_e32 v129, 0xffff0000, v218
	v_exp_f32_e32 v34, v33
	v_mul_f32_e32 v33, v226, v35
	v_pk_fma_f32 v[120:121], v[120:121], v[128:129], v[124:125]
	v_lshlrev_b32_e32 v124, 16, v216
	v_and_b32_e32 v125, 0xffff0000, v216
	v_mul_f32_e32 v28, v226, v28
	v_pk_fma_f32 v[116:117], v[116:117], v[124:125], v[120:121]
	v_lshlrev_b32_e32 v120, 16, v223
	v_and_b32_e32 v121, 0xffff0000, v223
	v_exp_f32_e32 v35, v33
	v_mul_f32_e32 v29, v226, v29
	v_pk_fma_f32 v[120:121], v[130:131], v[120:121], 0 op_sel_hi:[1,1,0]
	v_lshlrev_b32_e32 v124, 16, v221
	v_and_b32_e32 v125, 0xffff0000, v221
	v_exp_f32_e32 v28, v28
	v_pk_fma_f32 v[120:121], v[126:127], v[124:125], v[120:121]
	v_lshlrev_b32_e32 v124, 16, v219
	v_and_b32_e32 v125, 0xffff0000, v219
	v_exp_f32_e32 v29, v29
	v_pk_fma_f32 v[120:121], v[122:123], v[124:125], v[120:121]
	v_lshlrev_b32_e32 v122, 16, v217
	v_and_b32_e32 v123, 0xffff0000, v217
	v_rcp_f32_e32 v33, v2
	v_add_f32_e32 v2, 1.0, v34
	v_ashrrev_i32_e32 v215, 31, v214
	v_pk_fma_f32 v[118:119], v[118:119], v[122:123], v[120:121]
	v_cvt_pk_bf16_f32 v120, v116, v117
	v_lshlrev_b64 v[116:117], 11, v[212:213]
	v_rcp_f32_e32 v34, v2
	v_add_f32_e32 v2, 1.0, v35
	v_cvt_pk_bf16_f32 v121, v118, v119
	v_lshl_add_u64 v[116:117], s[14:15], 0, v[116:117]
	v_lshlrev_b64 v[118:119], 1, v[214:215]
	v_rcp_f32_e32 v35, v2
	v_add_f32_e32 v2, 1.0, v28
	v_lshl_add_u64 v[116:117], v[116:117], 0, v[118:119]
	v_rcp_f32_e32 v28, v2
	v_add_f32_e32 v2, 1.0, v29
	v_mul_f32_e32 v29, v226, v30
	global_store_dwordx2 v[116:117], v[120:121], off nt
	v_lshlrev_b32_e32 v120, 16, v204
	v_and_b32_e32 v121, 0xffff0000, v204
	v_pk_fma_f32 v[112:113], v[112:113], v[120:121], 0 op_sel_hi:[1,1,0]
	v_lshlrev_b32_e32 v120, 16, v210
	v_and_b32_e32 v121, 0xffff0000, v210
	v_exp_f32_e32 v30, v29
	v_mul_f32_e32 v29, v226, v31
	v_pk_fma_f32 v[108:109], v[108:109], v[120:121], v[112:113]
	v_lshlrev_b32_e32 v112, 16, v208
	v_and_b32_e32 v113, 0xffff0000, v208
	v_mul_f32_e32 v24, v226, v24
	v_pk_fma_f32 v[104:105], v[104:105], v[112:113], v[108:109]
	v_lshlrev_b32_e32 v108, 16, v206
	v_and_b32_e32 v109, 0xffff0000, v206
	v_exp_f32_e32 v31, v29
	v_mul_f32_e32 v25, v226, v25
	v_pk_fma_f32 v[100:101], v[100:101], v[108:109], v[104:105]
	v_lshlrev_b32_e32 v104, 16, v205
	v_and_b32_e32 v105, 0xffff0000, v205
	v_exp_f32_e32 v24, v24
	v_pk_fma_f32 v[104:105], v[114:115], v[104:105], 0 op_sel_hi:[1,1,0]
	v_lshlrev_b32_e32 v108, 16, v211
	v_and_b32_e32 v109, 0xffff0000, v211
	v_exp_f32_e32 v25, v25
	v_pk_fma_f32 v[104:105], v[110:111], v[108:109], v[104:105]
	v_lshlrev_b32_e32 v108, 16, v209
	v_and_b32_e32 v109, 0xffff0000, v209
	v_rcp_f32_e32 v29, v2
	v_add_f32_e32 v2, 1.0, v30
	v_pk_fma_f32 v[104:105], v[106:107], v[108:109], v[104:105]
	v_lshlrev_b32_e32 v106, 16, v207
	v_and_b32_e32 v107, 0xffff0000, v207
	v_rcp_f32_e32 v30, v2
	v_add_f32_e32 v2, 1.0, v31
	v_pk_fma_f32 v[102:103], v[102:103], v[106:107], v[104:105]
	v_rcp_f32_e32 v31, v2
	v_add_f32_e32 v2, 1.0, v24
	v_cvt_pk_bf16_f32 v100, v100, v101
	v_cvt_pk_bf16_f32 v101, v102, v103
	v_lshlrev_b64 v[102:103], 11, v[194:195]
	v_rcp_f32_e32 v24, v2
	v_add_f32_e32 v2, 1.0, v25
	v_mul_f32_e32 v25, v226, v26
	v_lshl_add_u64 v[102:103], s[14:15], 0, v[102:103]
	v_lshl_add_u64 v[102:103], v[102:103], 0, v[118:119]
	v_exp_f32_e32 v26, v25
	v_mul_f32_e32 v25, v226, v27
	global_store_dwordx2 v[102:103], v[100:101], off nt
	v_lshlrev_b32_e32 v100, 16, v192
	v_and_b32_e32 v101, 0xffff0000, v192
	v_mul_f32_e32 v20, v226, v20
	v_pk_fma_f32 v[96:97], v[96:97], v[100:101], 0 op_sel_hi:[1,1,0]
	v_lshlrev_b32_e32 v100, 16, v190
	v_and_b32_e32 v101, 0xffff0000, v190
	v_exp_f32_e32 v27, v25
	v_mul_f32_e32 v21, v226, v21
	v_pk_fma_f32 v[92:93], v[92:93], v[100:101], v[96:97]
	v_lshlrev_b32_e32 v96, 16, v188
	v_and_b32_e32 v97, 0xffff0000, v188
	v_exp_f32_e32 v20, v20
	v_pk_fma_f32 v[88:89], v[88:89], v[96:97], v[92:93]
	v_lshlrev_b32_e32 v92, 16, v186
	v_and_b32_e32 v93, 0xffff0000, v186
	v_exp_f32_e32 v21, v21
	v_pk_fma_f32 v[84:85], v[84:85], v[92:93], v[88:89]
	v_lshlrev_b32_e32 v88, 16, v193
	v_and_b32_e32 v89, 0xffff0000, v193
	v_rcp_f32_e32 v25, v2
	v_add_f32_e32 v2, 1.0, v26
	v_pk_fma_f32 v[88:89], v[98:99], v[88:89], 0 op_sel_hi:[1,1,0]
	v_lshlrev_b32_e32 v92, 16, v191
	v_and_b32_e32 v93, 0xffff0000, v191
	v_rcp_f32_e32 v26, v2
	v_add_f32_e32 v2, 1.0, v27
	v_pk_fma_f32 v[88:89], v[94:95], v[92:93], v[88:89]
	v_lshlrev_b32_e32 v92, 16, v189
	v_and_b32_e32 v93, 0xffff0000, v189
	v_rcp_f32_e32 v27, v2
	v_add_f32_e32 v2, 1.0, v20
	v_pk_fma_f32 v[88:89], v[90:91], v[92:93], v[88:89]
	v_lshlrev_b32_e32 v90, 16, v187
	v_and_b32_e32 v91, 0xffff0000, v187
	v_rcp_f32_e32 v20, v2
	v_add_f32_e32 v2, 1.0, v21
	v_pk_fma_f32 v[86:87], v[86:87], v[90:91], v[88:89]
	v_rcp_f32_e32 v21, v2
	v_mul_f32_e32 v2, v226, v22
	v_cvt_pk_bf16_f32 v84, v84, v85
	v_cvt_pk_bf16_f32 v85, v86, v87
	v_lshlrev_b64 v[86:87], 11, v[184:185]
	v_mul_f32_e32 v22, v226, v23
	v_lshl_add_u64 v[86:87], s[14:15], 0, v[86:87]
	v_exp_f32_e32 v2, v2
	v_lshl_add_u64 v[86:87], v[86:87], 0, v[118:119]
	v_exp_f32_e32 v23, v22
	global_store_dwordx2 v[86:87], v[84:85], off nt
	v_lshlrev_b32_e32 v84, 16, v180
	v_and_b32_e32 v85, 0xffff0000, v180
	v_pk_fma_f32 v[80:81], v[80:81], v[84:85], 0 op_sel_hi:[1,1,0]
	v_lshlrev_b32_e32 v84, 16, v178
	v_and_b32_e32 v85, 0xffff0000, v178
	v_pk_fma_f32 v[76:77], v[76:77], v[84:85], v[80:81]
	v_lshlrev_b32_e32 v80, 16, v176
	v_and_b32_e32 v81, 0xffff0000, v176
	v_add_f32_e32 v2, 1.0, v2
	v_pk_fma_f32 v[72:73], v[72:73], v[80:81], v[76:77]
	v_lshlrev_b32_e32 v76, 16, v182
	v_and_b32_e32 v77, 0xffff0000, v182
	v_rcp_f32_e32 v22, v2
	v_add_f32_e32 v2, 1.0, v23
	v_pk_fma_f32 v[68:69], v[68:69], v[76:77], v[72:73]
	v_lshlrev_b32_e32 v72, 16, v181
	v_and_b32_e32 v73, 0xffff0000, v181
	v_rcp_f32_e32 v23, v2
	s_waitcnt vmcnt(7)
	v_mul_f32_e32 v2, v225, v16
	v_pk_fma_f32 v[72:73], v[82:83], v[72:73], 0 op_sel_hi:[1,1,0]
	v_lshlrev_b32_e32 v76, 16, v179
	v_and_b32_e32 v77, 0xffff0000, v179
	v_mul_f32_e32 v16, v225, v17
	v_pk_fma_f32 v[72:73], v[78:79], v[76:77], v[72:73]
	v_lshlrev_b32_e32 v76, 16, v177
	v_and_b32_e32 v77, 0xffff0000, v177
	v_exp_f32_e32 v2, v2
	v_pk_fma_f32 v[72:73], v[74:75], v[76:77], v[72:73]
	v_lshlrev_b32_e32 v74, 16, v183
	v_and_b32_e32 v75, 0xffff0000, v183
	v_exp_f32_e32 v17, v16
	v_pk_fma_f32 v[70:71], v[70:71], v[74:75], v[72:73]
	v_cvt_pk_bf16_f32 v68, v68, v69
	v_cvt_pk_bf16_f32 v69, v70, v71
	v_lshlrev_b64 v[70:71], 11, v[174:175]
	v_lshl_add_u64 v[70:71], s[14:15], 0, v[70:71]
	v_add_f32_e32 v2, 1.0, v2
	v_lshl_add_u64 v[70:71], v[70:71], 0, v[118:119]
	v_rcp_f32_e32 v16, v2
	v_add_f32_e32 v2, 1.0, v17
	v_mul_f32_e32 v17, v225, v18
	global_store_dwordx2 v[70:71], v[68:69], off nt
	v_lshlrev_b32_e32 v68, 16, v170
	v_and_b32_e32 v69, 0xffff0000, v170
	v_pk_fma_f32 v[64:65], v[64:65], v[68:69], 0 op_sel_hi:[1,1,0]
	v_lshlrev_b32_e32 v68, 16, v168
	v_and_b32_e32 v69, 0xffff0000, v168
	v_exp_f32_e32 v18, v17
	v_mul_f32_e32 v17, v225, v19
	v_pk_fma_f32 v[60:61], v[60:61], v[68:69], v[64:65]
	v_lshlrev_b32_e32 v64, 16, v166
	v_and_b32_e32 v65, 0xffff0000, v166
	v_mul_f32_e32 v12, v225, v12
	v_pk_fma_f32 v[56:57], v[56:57], v[64:65], v[60:61]
	v_lshlrev_b32_e32 v60, 16, v172
	v_and_b32_e32 v61, 0xffff0000, v172
	v_exp_f32_e32 v19, v17
	v_mul_f32_e32 v13, v225, v13
	v_pk_fma_f32 v[52:53], v[52:53], v[60:61], v[56:57]
	v_lshlrev_b32_e32 v56, 16, v171
	v_and_b32_e32 v57, 0xffff0000, v171
	v_exp_f32_e32 v12, v12
	v_pk_fma_f32 v[56:57], v[66:67], v[56:57], 0 op_sel_hi:[1,1,0]
	v_lshlrev_b32_e32 v60, 16, v169
	v_and_b32_e32 v61, 0xffff0000, v169
	v_exp_f32_e32 v13, v13
	v_pk_fma_f32 v[56:57], v[62:63], v[60:61], v[56:57]
	v_lshlrev_b32_e32 v60, 16, v167
	v_and_b32_e32 v61, 0xffff0000, v167
	v_rcp_f32_e32 v17, v2
	v_add_f32_e32 v2, 1.0, v18
	v_pk_fma_f32 v[56:57], v[58:59], v[60:61], v[56:57]
	v_lshlrev_b32_e32 v58, 16, v173
	v_and_b32_e32 v59, 0xffff0000, v173
	v_rcp_f32_e32 v18, v2
	v_add_f32_e32 v2, 1.0, v19
	v_pk_fma_f32 v[54:55], v[54:55], v[58:59], v[56:57]
	v_rcp_f32_e32 v19, v2
	v_add_f32_e32 v2, 1.0, v12
	v_cvt_pk_bf16_f32 v52, v52, v53
	v_cvt_pk_bf16_f32 v53, v54, v55
	v_lshlrev_b64 v[54:55], 11, v[164:165]
	v_rcp_f32_e32 v12, v2
	v_add_f32_e32 v2, 1.0, v13
	v_mul_f32_e32 v13, v225, v14
	v_lshl_add_u64 v[54:55], s[14:15], 0, v[54:55]
	v_lshl_add_u64 v[54:55], v[54:55], 0, v[118:119]
	v_exp_f32_e32 v14, v13
	v_mul_f32_e32 v13, v225, v15
	global_store_dwordx2 v[54:55], v[52:53], off nt
	v_lshlrev_b32_e32 v52, 16, v158
	v_and_b32_e32 v53, 0xffff0000, v158
	v_mul_f32_e32 v8, v225, v8
	v_pk_fma_f32 v[48:49], v[48:49], v[52:53], 0 op_sel_hi:[1,1,0]
	v_lshlrev_b32_e32 v52, 16, v156
	v_and_b32_e32 v53, 0xffff0000, v156
	v_exp_f32_e32 v15, v13
	v_mul_f32_e32 v9, v225, v9
	v_pk_fma_f32 v[44:45], v[44:45], v[52:53], v[48:49]
	v_lshlrev_b32_e32 v48, 16, v162
	v_and_b32_e32 v49, 0xffff0000, v162
	v_exp_f32_e32 v8, v8
	v_pk_fma_f32 v[40:41], v[40:41], v[48:49], v[44:45]
	v_lshlrev_b32_e32 v44, 16, v160
	v_and_b32_e32 v45, 0xffff0000, v160
	v_exp_f32_e32 v9, v9
	v_pk_fma_f32 v[36:37], v[36:37], v[44:45], v[40:41]
	v_lshlrev_b32_e32 v40, 16, v159
	v_and_b32_e32 v41, 0xffff0000, v159
	v_rcp_f32_e32 v13, v2
	v_add_f32_e32 v2, 1.0, v14
	v_pk_fma_f32 v[40:41], v[50:51], v[40:41], 0 op_sel_hi:[1,1,0]
	v_lshlrev_b32_e32 v44, 16, v157
	v_and_b32_e32 v45, 0xffff0000, v157
	v_rcp_f32_e32 v14, v2
	v_add_f32_e32 v2, 1.0, v15
	v_pk_fma_f32 v[40:41], v[46:47], v[44:45], v[40:41]
	v_lshlrev_b32_e32 v44, 16, v163
	v_and_b32_e32 v45, 0xffff0000, v163
	v_rcp_f32_e32 v15, v2
	v_add_f32_e32 v2, 1.0, v8
	v_pk_fma_f32 v[40:41], v[42:43], v[44:45], v[40:41]
	v_lshlrev_b32_e32 v42, 16, v161
	v_and_b32_e32 v43, 0xffff0000, v161
	v_rcp_f32_e32 v8, v2
	v_add_f32_e32 v2, 1.0, v9
	v_mul_f32_e32 v9, v225, v10
	v_pk_fma_f32 v[38:39], v[38:39], v[42:43], v[40:41]
	s_mov_b32 s4, 0x48000
	v_cvt_pk_bf16_f32 v36, v36, v37
	v_cvt_pk_bf16_f32 v37, v38, v39
	v_add_co_u32_e32 v38, vcc, s4, v116
	v_exp_f32_e32 v10, v9
	v_mul_f32_e32 v9, v225, v11
	v_addc_co_u32_e32 v39, vcc, 0, v117, vcc
	v_mul_f32_e32 v4, v225, v4
	global_store_dwordx2 v[38:39], v[36:37], off nt
	v_lshlrev_b32_e32 v36, 16, v148
	v_and_b32_e32 v37, 0xffff0000, v148
	v_exp_f32_e32 v11, v9
	v_mul_f32_e32 v5, v225, v5
	v_pk_fma_f32 v[32:33], v[32:33], v[36:37], 0 op_sel_hi:[1,1,0]
	v_lshlrev_b32_e32 v36, 16, v154
	v_and_b32_e32 v37, 0xffff0000, v154
	v_exp_f32_e32 v4, v4
	v_pk_fma_f32 v[28:29], v[28:29], v[36:37], v[32:33]
	v_lshlrev_b32_e32 v32, 16, v152
	v_and_b32_e32 v33, 0xffff0000, v152
	v_exp_f32_e32 v5, v5
	v_pk_fma_f32 v[24:25], v[24:25], v[32:33], v[28:29]
	v_lshlrev_b32_e32 v28, 16, v150
	v_and_b32_e32 v29, 0xffff0000, v150
	v_rcp_f32_e32 v9, v2
	v_add_f32_e32 v2, 1.0, v10
	v_pk_fma_f32 v[20:21], v[20:21], v[28:29], v[24:25]
	v_lshlrev_b32_e32 v24, 16, v149
	v_and_b32_e32 v25, 0xffff0000, v149
	v_rcp_f32_e32 v10, v2
	v_add_f32_e32 v2, 1.0, v11
	v_pk_fma_f32 v[24:25], v[34:35], v[24:25], 0 op_sel_hi:[1,1,0]
	v_lshlrev_b32_e32 v28, 16, v155
	v_and_b32_e32 v29, 0xffff0000, v155
	v_rcp_f32_e32 v11, v2
	v_add_f32_e32 v2, 1.0, v4
	v_pk_fma_f32 v[24:25], v[30:31], v[28:29], v[24:25]
	v_lshlrev_b32_e32 v28, 16, v153
	v_and_b32_e32 v29, 0xffff0000, v153
	v_rcp_f32_e32 v4, v2
	v_add_f32_e32 v2, 1.0, v5
	v_pk_fma_f32 v[24:25], v[26:27], v[28:29], v[24:25]
	v_lshlrev_b32_e32 v26, 16, v151
	v_and_b32_e32 v27, 0xffff0000, v151
	v_rcp_f32_e32 v5, v2
	v_mul_f32_e32 v2, v225, v6
	v_pk_fma_f32 v[22:23], v[22:23], v[26:27], v[24:25]
	s_mov_b32 s4, 0x50000
	v_mul_f32_e32 v6, v225, v7
	v_cvt_pk_bf16_f32 v20, v20, v21
	v_cvt_pk_bf16_f32 v21, v22, v23
	v_add_co_u32_e32 v22, vcc, s4, v116
	v_exp_f32_e32 v2, v2
	v_addc_co_u32_e32 v23, vcc, 0, v117, vcc
	v_exp_f32_e32 v7, v6
	global_store_dwordx2 v[22:23], v[20:21], off nt
	s_waitcnt vmcnt(10)
	v_lshlrev_b32_e32 v20, 16, v146
	v_and_b32_e32 v21, 0xffff0000, v146
	v_pk_fma_f32 v[16:17], v[16:17], v[20:21], 0 op_sel_hi:[1,1,0]
	s_waitcnt vmcnt(9)
	v_lshlrev_b32_e32 v20, 16, v144
	v_and_b32_e32 v21, 0xffff0000, v144
	v_pk_fma_f32 v[12:13], v[12:13], v[20:21], v[16:17]
	s_waitcnt vmcnt(8)
	v_lshlrev_b32_e32 v16, 16, v142
	v_and_b32_e32 v17, 0xffff0000, v142
	v_add_f32_e32 v2, 1.0, v2
	v_pk_fma_f32 v[8:9], v[8:9], v[16:17], v[12:13]
	s_waitcnt vmcnt(7)
	v_lshlrev_b32_e32 v12, 16, v140
	v_and_b32_e32 v13, 0xffff0000, v140
	v_rcp_f32_e32 v6, v2
	v_add_f32_e32 v2, 1.0, v7
	v_pk_fma_f32 v[4:5], v[4:5], v[12:13], v[8:9]
	v_rcp_f32_e32 v7, v2
	v_lshlrev_b32_e32 v8, 16, v147
	v_and_b32_e32 v9, 0xffff0000, v147
	v_pk_fma_f32 v[8:9], v[18:19], v[8:9], 0 op_sel_hi:[1,1,0]
	v_lshlrev_b32_e32 v12, 16, v145
	v_and_b32_e32 v13, 0xffff0000, v145
	v_pk_fma_f32 v[8:9], v[14:15], v[12:13], v[8:9]
	v_lshlrev_b32_e32 v12, 16, v143
	v_and_b32_e32 v13, 0xffff0000, v143
	v_pk_fma_f32 v[8:9], v[10:11], v[12:13], v[8:9]
	v_lshlrev_b32_e32 v10, 16, v141
	v_and_b32_e32 v11, 0xffff0000, v141
	v_pk_fma_f32 v[6:7], v[6:7], v[10:11], v[8:9]
	v_cvt_pk_bf16_f32 v4, v4, v5
	v_cvt_pk_bf16_f32 v5, v6, v7
	v_add_co_u32_e32 v6, vcc, 0x58000, v116
	s_mov_b64 s[4:5], -1
	s_nop 0
	v_addc_co_u32_e32 v7, vcc, 0, v117, vcc
	s_andn2_b64 vcc, exec, s[38:39]
	s_mov_b32 s77, 0xc000
	s_mov_b32 s76, 0xe000
	s_movk_i32 s75, 0x3400
	v_readlane_b32 s74, v255, 38
	global_store_dwordx2 v[6:7], v[4:5], off nt
	s_cbranch_vccnz .LBB0_1036
	s_andn2_b64 vcc, exec, s[10:11]
	s_cbranch_vccnz .LBB0_1035
	s_barrier
	s_branch .LBB0_1035
